# v31
# speedup vs baseline: 1.1158x; 1.0081x over previous
.LBB3_86:
	s_and_b64 vcc, exec, s[0:1]
	s_cbranch_vccz .LBB3_222
	v_ashrrev_i32_e32 v10, 3, v189
	v_add_u32_e32 v10, s22, v10
	v_min_i32_e32 v10, 0xc34f, v10
	v_and_b32_e32 v11, 7, v189
	v_lshl_or_b32 v176, v10, 3, v11
	v_lshl_add_u64 v[10:11], v[176:177], 2, s[62:63]
	global_load_dword v227, v[10:11], off
	v_ashrrev_i32_e32 v0, 1, v189
	s_add_i32 s79, s23, -1
	v_add_u32_e32 v5, 32, v0
	v_add_u32_e32 v7, 64, v0
	v_add_u32_e32 v2, 0x60, v0
	v_min_i32_e32 v9, s79, v0
	v_min_i32_e32 v5, s79, v5
	v_min_i32_e32 v7, s79, v7
	v_min_i32_e32 v2, s79, v2
	v_add_lshl_u32 v9, v9, s78, 2
	v_add_lshl_u32 v5, v5, s78, 2
	v_add_lshl_u32 v7, v7, s78, 2
	v_add_lshl_u32 v2, v2, s78, 2
	global_load_dword v9, v9, s[58:59]
	global_load_dword v5, v5, s[58:59]
	global_load_dword v7, v7, s[58:59]
	global_load_dword v2, v2, s[58:59]
.LBB3_95:
	v_and_b32_e32 v8, 1, v189
	v_cmp_eq_u32_e64 s[4:5], 0, v8
	v_lshl_add_u32 v1, v8, 4, s88
	s_waitcnt vmcnt(0)
	v_lshl_or_b32 v176, v9, 1, v8
	v_lshl_add_u64 v[10:11], v[176:177], 4, s[60:61]
	global_load_dwordx4 v[12:15], v[10:11], off
	v_lshl_or_b32 v176, v5, 1, v8
	v_lshl_add_u64 v[10:11], v[176:177], 4, s[60:61]
	global_load_dwordx4 v[16:19], v[10:11], off
	v_lshl_or_b32 v176, v7, 1, v8
	v_lshl_add_u64 v[10:11], v[176:177], 4, s[60:61]
	global_load_dwordx4 v[20:23], v[10:11], off
	v_lshl_or_b32 v176, v2, 1, v8
	v_lshl_add_u64 v[10:11], v[176:177], 4, s[60:61]
	global_load_dwordx4 v[24:27], v[10:11], off
	v_lshl_add_u32 v10, v0, 2, s90
	v_lshl_add_u32 v11, v0, 5, v1
	ds_write_b32 v10, v9
	ds_write_b32 v10, v5 offset:128
	ds_write_b32 v10, v7 offset:256
	ds_write_b32 v10, v2 offset:384
	s_waitcnt vmcnt(3)
	ds_write_b128 v11, v[12:15]
	s_waitcnt vmcnt(2)
	ds_write_b128 v11, v[16:19] offset:1024
	s_waitcnt vmcnt(1)
	ds_write_b128 v11, v[20:23] offset:2048
	s_waitcnt vmcnt(0)
	ds_write_b128 v11, v[24:27] offset:3072
	s_mov_b64 s[0:1], 0

.LBB3_129:
	v_mov_b32_e32 v162, v227
	v_subrev_u32_e32 v164, s78, v160
	v_lshl_add_u32 v171, v193, 2, s88
	v_lshl_add_u32 v237, v164, 5, v171
	ds_read_b32 v173, v237 offset:32
	ds_read_b32 v174, v237 offset:64
	ds_read_b32 v175, v237 offset:96
	ds_read_b32 v176, v237 offset:128
	ds_read_b32 v195, v237 offset:160
	ds_read_b32 v196, v237 offset:192
	ds_read_b32 v197, v237 offset:224
	ds_read_b32 v198, v237 offset:256
	ds_read_b32 v199, v237 offset:288
	ds_read_b32 v200, v237 offset:320
	ds_read_b32 v201, v237 offset:352
	ds_read_b32 v202, v237 offset:384
	ds_read_b32 v203, v237 offset:416
	ds_read_b32 v204, v237 offset:448
	ds_read_b32 v205, v237 offset:480
	ds_read_b32 v206, v237 offset:512
	ds_read_b32 v207, v237 offset:544
	ds_read_b32 v208, v237 offset:576
	ds_read_b32 v209, v237 offset:608
	ds_read_b32 v210, v237 offset:640
	ds_read_b32 v211, v237 offset:672
	ds_read_b32 v170, v237 offset:704
	ds_read_b32 v163, v237 offset:736
	v_sub_u32_e32 v166, v161, v160
	v_cmp_lt_i32_e64 s[44:45], 0, v166
	v_mov_b32_e32 v172, 0xff800000
	s_and_saveexec_b64 s[0:1], s[44:45]
	s_cbranch_execz .LBB3_131
	v_min_i32_e32 v161, 0x7f, v164
	v_lshl_add_u32 v161, v161, 5, v171
	ds_read_b32 v161, v161
	s_waitcnt lgkmcnt(0)
	v_add_f32_e32 v161, v162, v161
	v_mul_f32_e32 v172, 0x3e4ccccd, v161
	s_nop 1
	v_max_f32_e32 v172, v161, v172
.LBB3_131:
	s_or_b64 exec, exec, s[0:1]
	s_waitcnt lgkmcnt(14)
	v_add_f32_e32 v161, v162, v173
	v_mul_f32_e32 v173, 0x3e4ccccd, v161
	v_add_f32_e32 v174, v162, v174
	v_mul_f32_e32 v212, 0x3e4ccccd, v174
	v_max_f32_e32 v161, v161, v173
	v_add_f32_e32 v175, v162, v175
	v_add_f32_e32 v176, v162, v176
	v_max_f32_e32 v174, v174, v212
	v_mul_f32_e32 v212, 0x3e4ccccd, v175
	v_add_f32_e32 v195, v162, v195
	v_add_f32_e32 v196, v162, v196
	v_max_f32_e32 v175, v175, v212
	v_mul_f32_e32 v212, 0x3e4ccccd, v176
	v_add_f32_e32 v197, v162, v197
	v_add_f32_e32 v198, v162, v198
	v_max_f32_e32 v176, v176, v212
	v_mul_f32_e32 v212, 0x3e4ccccd, v195
	v_add_f32_e32 v199, v162, v199
	s_waitcnt lgkmcnt(13)
	v_add_f32_e32 v200, v162, v200
	v_max_f32_e32 v195, v195, v212
	v_mul_f32_e32 v212, 0x3e4ccccd, v196
	s_waitcnt lgkmcnt(12)
	v_add_f32_e32 v201, v162, v201
	s_waitcnt lgkmcnt(11)
	v_add_f32_e32 v202, v162, v202
	v_max_f32_e32 v196, v196, v212
	v_mul_f32_e32 v212, 0x3e4ccccd, v197
	s_waitcnt lgkmcnt(10)
	v_add_f32_e32 v203, v162, v203
	s_waitcnt lgkmcnt(9)
	v_add_f32_e32 v204, v162, v204
	v_max_f32_e32 v197, v197, v212
	v_mul_f32_e32 v212, 0x3e4ccccd, v198
	v_cmp_lt_i32_e64 s[50:51], 1, v166
	s_waitcnt lgkmcnt(8)
	v_add_f32_e32 v205, v162, v205
	v_max_f32_e32 v198, v198, v212
	v_mul_f32_e32 v212, 0x3e4ccccd, v199
	v_cndmask_b32_e64 v173, v181, v161, s[50:51]
	v_cmp_lt_i32_e64 s[48:49], 2, v166
	v_max_f32_e32 v199, v199, v212
	v_mul_f32_e32 v212, 0x3e4ccccd, v200
	v_cmp_lt_i32_e64 s[46:47], 3, v166
	s_waitcnt lgkmcnt(7)
	v_add_f32_e32 v206, v162, v206
	v_max_f32_e32 v200, v200, v212
	v_mul_f32_e32 v212, 0x3e4ccccd, v201
	v_max3_f32 v161, v172, s91, v173
	v_cndmask_b32_e64 v174, v181, v174, s[48:49]
	v_max_f32_e32 v201, v201, v212
	v_mul_f32_e32 v212, 0x3e4ccccd, v202
	v_cndmask_b32_e64 v175, v181, v175, s[46:47]
	v_cmp_lt_i32_e64 s[42:43], 4, v166
	v_max_f32_e32 v202, v202, v212
	v_mul_f32_e32 v212, 0x3e4ccccd, v203
	v_cmp_lt_i32_e64 s[40:41], 5, v166
	s_waitcnt lgkmcnt(6)
	v_add_f32_e32 v207, v162, v207
	v_max_f32_e32 v203, v203, v212
	v_mul_f32_e32 v212, 0x3e4ccccd, v204
	v_max3_f32 v161, v161, v174, v175
	v_cndmask_b32_e64 v176, v181, v176, s[42:43]
	v_max_f32_e32 v204, v204, v212
	v_mul_f32_e32 v212, 0x3e4ccccd, v205
	v_cndmask_b32_e64 v195, v181, v195, s[40:41]
	v_cmp_lt_i32_e64 s[38:39], 6, v166
	v_max_f32_e32 v205, v205, v212
	v_mul_f32_e32 v212, 0x3e4ccccd, v206
	v_cmp_lt_i32_e64 s[36:37], 7, v166
	s_waitcnt lgkmcnt(5)
	v_add_f32_e32 v208, v162, v208
	v_max_f32_e32 v206, v206, v212
	v_mul_f32_e32 v212, 0x3e4ccccd, v207
	v_max3_f32 v161, v161, v176, v195
	v_cndmask_b32_e64 v196, v181, v196, s[38:39]
	v_cndmask_b32_e64 v197, v181, v197, s[36:37]
	v_cmp_lt_i32_e64 s[34:35], 8, v166
	v_cmp_lt_i32_e64 s[30:31], 9, v166
	v_max_f32_e32 v207, v207, v212
	v_mul_f32_e32 v212, 0x3e4ccccd, v208
	s_waitcnt lgkmcnt(4)
	v_add_f32_e32 v209, v162, v209
	v_max3_f32 v161, v161, v196, v197
	v_cndmask_b32_e64 v198, v181, v198, s[34:35]
	v_cndmask_b32_e64 v199, v181, v199, s[30:31]
	v_cmp_lt_i32_e64 s[28:29], 10, v166
	v_cmp_lt_i32_e64 s[26:27], 11, v166
	v_max_f32_e32 v208, v208, v212
	v_mul_f32_e32 v212, 0x3e4ccccd, v209
	s_waitcnt lgkmcnt(3)
	v_add_f32_e32 v210, v162, v210
	v_max3_f32 v161, v161, v198, v199
	v_cndmask_b32_e64 v200, v181, v200, s[28:29]
	v_cndmask_b32_e64 v201, v181, v201, s[26:27]
	v_cmp_lt_i32_e64 s[24:25], 12, v166
	v_cmp_lt_i32_e64 s[22:23], 13, v166
	v_max_f32_e32 v209, v209, v212
	v_mul_f32_e32 v212, 0x3e4ccccd, v210
	s_waitcnt lgkmcnt(2)
	v_add_f32_e32 v211, v162, v211
	v_max3_f32 v161, v161, v200, v201
	v_cndmask_b32_e64 v202, v181, v202, s[24:25]
	v_cndmask_b32_e64 v203, v181, v203, s[22:23]
	v_cmp_lt_i32_e64 s[20:21], 14, v166
	v_cmp_lt_i32_e64 s[18:19], 15, v166
	v_max_f32_e32 v210, v210, v212
	v_mul_f32_e32 v212, 0x3e4ccccd, v211
	s_waitcnt lgkmcnt(1)
	v_add_f32_e32 v170, v162, v170
	v_max3_f32 v161, v161, v202, v203
	v_cndmask_b32_e64 v204, v181, v204, s[20:21]
	v_cndmask_b32_e64 v205, v181, v205, s[18:19]
	v_cmp_lt_i32_e64 s[16:17], 16, v166
	v_cmp_lt_i32_e64 s[14:15], 17, v166
	v_max_f32_e32 v211, v211, v212
	v_mul_f32_e32 v212, 0x3e4ccccd, v170
	v_max3_f32 v161, v161, v204, v205
	v_cndmask_b32_e64 v206, v181, v206, s[16:17]
	v_cndmask_b32_e64 v207, v181, v207, s[14:15]
	v_cmp_lt_i32_e64 s[12:13], 18, v166
	v_cmp_lt_i32_e64 s[10:11], 19, v166
	v_max_f32_e32 v170, v170, v212
	v_cmp_lt_i32_e64 s[4:5], 22, v166
	s_waitcnt lgkmcnt(0)
	v_add_f32_e32 v163, v162, v163
	v_max3_f32 v161, v161, v206, v207
	v_cndmask_b32_e64 v208, v181, v208, s[12:13]
	v_cndmask_b32_e64 v209, v181, v209, s[10:11]
	v_cmp_lt_i32_e64 s[8:9], 20, v166
	v_cmp_lt_i32_e64 s[6:7], 21, v166
	v_cndmask_b32_e64 v212, v181, v170, s[4:5]
	v_mul_f32_e32 v170, 0x3e4ccccd, v163
	v_max3_f32 v161, v161, v208, v209
	v_cndmask_b32_e64 v210, v181, v210, s[8:9]
	v_cndmask_b32_e64 v211, v181, v211, s[6:7]
	v_max_f32_e32 v163, v163, v170
	v_cmp_lt_i32_e64 s[52:53], 23, v166
	v_max3_f32 v161, v161, v210, v211
	v_cmp_lt_i32_e64 s[0:1], 24, v166
	v_cndmask_b32_e64 v213, v181, v163, s[52:53]
	v_max3_f32 v170, v161, v212, v213
	s_and_saveexec_b64 s[70:71], s[0:1]
	s_cbranch_execz .LBB3_141
	v_subrev_u32_e32 v214, 24, v166
	v_mov_b32_e32 v161, 24
	v_cmp_lt_u32_e32 vcc, 1, v214
	s_mov_b64 s[82:83], -1
	s_and_saveexec_b64 s[80:81], vcc
	s_cbranch_execz .LBB3_136
	s_mov_b32 s92, s3
	s_mov_b32 s3, s66
	s_mov_b32 s67, s65
	s_mov_b32 s66, s64
	s_mov_b64 s[64:65], s[76:77]
	v_and_b32_e32 v215, -2, v214
	v_mov_b32_e32 v161, v164
	v_mov_b32_e32 v163, v162
	s_mov_b32 s69, 25
	s_mov_b32 s94, 24
	s_mov_b32 s89, 2
	s_mov_b64 s[84:85], 0
	v_mov_b32_e32 v218, v170
